# baseline (speedup 1.0000x reference)
.LBB3_5:
	s_or_b64 exec, exec, s[22:23]
	s_mov_b64 s[4:5], 0x10000
	s_mov_b64 s[4:5], 0x12000
	s_mov_b64 s[4:5], 0x14000
	s_mov_b64 s[4:5], 0x16000
	s_mov_b64 s[4:5], 0x18000
	s_mov_b64 s[4:5], 0x1a000
	s_mov_b64 s[4:5], 0x1c000
	s_mov_b64 s[4:5], 0x1e000
	v_lshlrev_b32_e32 v89, 4, v1
	s_mov_b64 s[6:7], 0
	s_mov_b64 s[4:5], -1
	v_mov_b32_e32 v19, v18
	v_mov_b32_e32 v20, v18
	v_mov_b32_e32 v21, v18
	v_mov_b32_e32 v84, v18
	v_mov_b32_e32 v85, v18
	v_mov_b32_e32 v86, v18
	v_mov_b32_e32 v87, v18
	v_mov_b32_e32 v40, 0xff800000
	v_mov_b32_e32 v41, v40
	v_mov_b32_e32 v42, v40
	v_mov_b32_e32 v43, v40
	v_mov_b32_e32 v44, v40
	v_mov_b32_e32 v45, v40
	v_mov_b32_e32 v46, v40
	v_mov_b32_e32 v47, v40
	v_mov_b32_e32 v48, v40
	v_mov_b32_e32 v49, v40
	v_mov_b32_e32 v50, v40
	v_mov_b32_e32 v51, v40
	v_mov_b32_e32 v52, v40
	v_mov_b32_e32 v53, v40
	v_mov_b32_e32 v54, v40
	v_mov_b32_e32 v55, v40
	v_mov_b32_e32 v56, 0
	v_mov_b32_e32 v57, 0
	v_mov_b32_e32 v58, 0
	v_mov_b32_e32 v59, 0
	v_mov_b32_e32 v60, 0
	v_mov_b32_e32 v61, 0
	v_mov_b32_e32 v62, 0
	v_mov_b32_e32 v63, 0
	s_waitcnt vmcnt(0)
	s_waitcnt lgkmcnt(0)
	s_barrier
	s_branch .LBB3_7
.LBB3_6:
	ds_read_b128 v[2:5], v89 offset:32768
	ds_read_b128 v[22:25], v89 offset:33792
	s_xor_b64 s[8:9], s[4:5], -1
	s_mov_b64 s[6:7], -1
	s_mov_b64 s[4:5], 0
	v_exp_f32_e32 v64, v42
	v_exp_f32_e32 v42, v44
	v_exp_f32_e32 v44, v46
	v_exp_f32_e32 v46, v47
	v_exp_f32_e32 v45, v45
	s_waitcnt lgkmcnt(1)
	v_mfma_f32_32x32x16_f16 v[2:17], v[2:5], v[72:75], 0
	s_and_b64 vcc, exec, s[8:9]
	v_exp_f32_e32 v47, v43
	v_exp_f32_e32 v40, v40
	v_exp_f32_e32 v65, v41
	v_cvt_pk_bf16_f32 v43, v44, v46
	v_cvt_pk_bf16_f32 v42, v42, v45
	s_waitcnt lgkmcnt(0)
	v_mfma_f32_32x32x16_f16 v[2:17], v[22:25], v[76:79], v[2:17]
	ds_read_b128 v[22:25], v89 offset:36864
	ds_read_b128 v[106:109], v89 offset:37888
	ds_read_b128 v[110:113], v89 offset:34816
	ds_read_b128 v[114:117], v89 offset:38912
	ds_read_b128 v[118:121], v89 offset:35840
	v_cvt_pk_bf16_f32 v41, v64, v47
	v_exp_f32_e32 v44, v48
	v_exp_f32_e32 v45, v50
	v_exp_f32_e32 v46, v52
	v_exp_f32_e32 v47, v54
	s_waitcnt lgkmcnt(4)
	v_mfma_f32_32x32x16_f16 v[24:39], v[22:25], v[72:75], 0
	v_exp_f32_e32 v48, v55
	v_exp_f32_e32 v50, v53
	v_exp_f32_e32 v51, v51
	v_exp_f32_e32 v49, v49
	v_cvt_pk_bf16_f32 v40, v40, v65
	s_waitcnt lgkmcnt(3)
	v_mfma_f32_32x32x16_f16 v[24:39], v[106:109], v[76:79], v[24:39]
	v_cvt_pk_bf16_f32 v47, v47, v48
	v_cvt_pk_bf16_f32 v46, v46, v50
	v_cvt_pk_bf16_f32 v45, v45, v51
	v_cvt_pk_bf16_f32 v44, v44, v49
	s_waitcnt lgkmcnt(2)
	v_mfma_f32_32x32x16_f16 v[2:17], v[110:113], v[80:83], v[2:17]
	v_permlane16_swap_b32_e32 v40, v44
	v_permlane16_swap_b32_e32 v41, v45
	v_permlane16_swap_b32_e32 v42, v46
	v_permlane16_swap_b32_e32 v43, v47
	s_waitcnt lgkmcnt(1)
	v_mfma_f32_32x32x16_f16 v[24:39], v[114:117], v[80:83], v[24:39]
	v_mfma_f32_16x16x32_bf16 v[84:87], v[56:59], v[40:43], v[18:21]
	v_mfma_f32_16x16x32_bf16 v[18:21], v[56:59], v[44:47], v[60:63]
	s_cmp_eq_u64 s[8:9], 0
	s_cbranch_scc0 .Lmy_attn_nodma
	s_mov_b32 m0, s48
	s_nop 0
	global_load_lds_dwordx4 v88, s[52:53]
	s_add_u32 s54, s52, 0x2000
	s_addc_u32 s55, s53, 0
	s_add_u32 m0, s48, 0x2000
	s_nop 0
	global_load_lds_dwordx4 v88, s[54:55]
	s_add_u32 s54, s52, 0x4000
	s_addc_u32 s55, s53, 0
	s_add_u32 m0, s48, 0x4000
	s_nop 0
	global_load_lds_dwordx4 v88, s[54:55]
	s_add_u32 s54, s52, 0x6000
	s_addc_u32 s55, s53, 0
	s_add_u32 m0, s48, 0x6000
	s_nop 0
	global_load_lds_dwordx4 v88, s[54:55]
	s_branch .Lmy_attn_dmadone

.Lmy_attn_dmadone:
	v_exp_f32_e32 v2, v2
	v_exp_f32_e32 v22, v3
	v_exp_f32_e32 v3, v4
	v_exp_f32_e32 v23, v5
	v_exp_f32_e32 v4, v6
	v_exp_f32_e32 v6, v7
	v_exp_f32_e32 v5, v8
	v_exp_f32_e32 v7, v9
	v_exp_f32_e32 v10, v10
	v_exp_f32_e32 v11, v11
	v_exp_f32_e32 v12, v12
	v_exp_f32_e32 v13, v13
	v_exp_f32_e32 v8, v14
	v_exp_f32_e32 v14, v15
	v_exp_f32_e32 v9, v16
	v_exp_f32_e32 v15, v17
	v_cvt_pk_bf16_f32 v5, v5, v7
	v_cvt_pk_bf16_f32 v4, v4, v6
	v_cvt_pk_bf16_f32 v3, v3, v23
	v_cvt_pk_bf16_f32 v2, v2, v22
	v_cvt_pk_bf16_f32 v9, v9, v15
	v_cvt_pk_bf16_f32 v8, v8, v14
	v_cvt_pk_bf16_f32 v7, v12, v13
	v_cvt_pk_bf16_f32 v6, v10, v11
	s_nop 1
	v_permlane16_swap_b32_e32 v2, v6
	v_permlane16_swap_b32_e32 v3, v7
	v_permlane16_swap_b32_e32 v4, v8
	v_permlane16_swap_b32_e32 v5, v9
	v_exp_f32_e32 v114, v24
	v_exp_f32_e32 v22, v26
	v_exp_f32_e32 v23, v28
	v_exp_f32_e32 v24, v30
	s_waitcnt lgkmcnt(0)
	v_mfma_f32_16x16x32_bf16 v[6:9], v[118:121], v[6:9], v[18:21]
	ds_read_b128 v[10:13], v89 offset:39936
	ds_read_b128 v[14:17], v89 offset:40960
	ds_read_b128 v[106:109], v89 offset:41984
	ds_read_b128 v[110:113], v89 offset:43008
	v_exp_f32_e32 v18, v31
	v_exp_f32_e32 v19, v29
	v_exp_f32_e32 v20, v27
	v_mfma_f32_16x16x32_bf16 v[2:5], v[118:121], v[2:5], v[84:87]
	s_nop 2
	v_exp_f32_e32 v84, v25
	v_cvt_pk_bf16_f32 v87, v24, v18
	v_cvt_pk_bf16_f32 v86, v23, v19
	v_cvt_pk_bf16_f32 v85, v22, v20
	s_waitcnt lgkmcnt(2)
	v_mfma_f32_32x32x16_f16 v[16:31], v[14:17], v[72:75], 0
	v_exp_f32_e32 v14, v32
	v_exp_f32_e32 v15, v34
	v_exp_f32_e32 v32, v36
	v_exp_f32_e32 v34, v37
	v_exp_f32_e32 v36, v38
	v_exp_f32_e32 v37, v39
	v_exp_f32_e32 v38, v35
	s_waitcnt lgkmcnt(1)
	v_mfma_f32_32x32x16_f16 v[16:31], v[106:109], v[76:79], v[16:31]
	v_exp_f32_e32 v39, v33
	v_cvt_pk_bf16_f32 v84, v114, v84
	v_cvt_pk_bf16_f32 v35, v36, v37
	v_cvt_pk_bf16_f32 v34, v32, v34
	v_cvt_pk_bf16_f32 v33, v15, v38
	v_cvt_pk_bf16_f32 v32, v14, v39
	s_nop 1
	v_permlane16_swap_b32_e32 v84, v32
	v_permlane16_swap_b32_e32 v85, v33
	v_permlane16_swap_b32_e32 v86, v34
	v_permlane16_swap_b32_e32 v87, v35
	ds_read_b128 v[36:39], v89 offset:44032
	s_nop 0
	v_mfma_f32_16x16x32_bf16 v[84:87], v[10:13], v[84:87], v[2:5]
	s_nop 2
	ds_read_b128 v[2:5], v89 offset:45056
	s_waitcnt lgkmcnt(2)
	v_mfma_f32_32x32x16_f16 v[16:31], v[110:113], v[80:83], v[16:31]
	v_mfma_f32_16x16x32_bf16 v[106:109], v[10:13], v[32:35], v[6:9]
	s_nop 10
	v_exp_f32_e32 v114, v16
	v_exp_f32_e32 v118, v17
	v_exp_f32_e32 v18, v18
	s_waitcnt lgkmcnt(0)
	v_mfma_f32_32x32x16_f16 v[2:17], v[2:5], v[72:75], 0
	v_exp_f32_e32 v20, v20
	v_exp_f32_e32 v21, v21
	v_exp_f32_e32 v19, v19
	ds_read_b128 v[32:35], v89 offset:46080
	ds_read_b128 v[110:113], v89 offset:47104
	v_cvt_pk_bf16_f32 v114, v114, v118
	v_cvt_pk_bf16_f32 v116, v20, v21
	v_cvt_pk_bf16_f32 v115, v18, v19
	ds_read_b128 v[118:121], v89 offset:48128
	ds_read_b128 v[18:21], v89 offset:49152
	v_exp_f32_e32 v22, v22
	v_exp_f32_e32 v23, v23
	s_waitcnt lgkmcnt(3)
	v_mfma_f32_32x32x16_f16 v[2:17], v[32:35], v[76:79], v[2:17]
	v_exp_f32_e32 v29, v29
	v_exp_f32_e32 v27, v27
	v_cvt_pk_bf16_f32 v117, v22, v23
	v_exp_f32_e32 v22, v24
	v_exp_f32_e32 v23, v26
	v_exp_f32_e32 v24, v28
	v_exp_f32_e32 v26, v30
	v_exp_f32_e32 v28, v31
	v_exp_f32_e32 v25, v25
	ds_read_b128 v[122:125], v89 offset:50176
	s_waitcnt lgkmcnt(3)
	v_mfma_f32_32x32x16_f16 v[2:17], v[110:113], v[80:83], v[2:17]
	v_cvt_pk_bf16_f32 v113, v26, v28
	v_cvt_pk_bf16_f32 v112, v24, v29
	v_cvt_pk_bf16_f32 v111, v23, v27
	v_cvt_pk_bf16_f32 v110, v22, v25
	s_nop 1
	v_permlane16_swap_b32_e32 v114, v110
	v_permlane16_swap_b32_e32 v115, v111
	s_waitcnt lgkmcnt(1)
	v_mfma_f32_32x32x16_f16 v[18:33], v[18:21], v[72:75], 0
	v_permlane16_swap_b32_e32 v116, v112
	v_permlane16_swap_b32_e32 v117, v113
	v_exp_f32_e32 v2, v2
	v_exp_f32_e32 v4, v4
	v_exp_f32_e32 v5, v5
	v_mfma_f32_16x16x32_bf16 v[84:87], v[36:39], v[114:117], v[84:87]
	v_exp_f32_e32 v3, v3
	v_exp_f32_e32 v6, v6
	v_exp_f32_e32 v7, v7
	v_mfma_f32_16x16x32_bf16 v[34:37], v[36:39], v[110:113], v[106:109]
	ds_read_b128 v[110:113], v89 offset:52224
	v_exp_f32_e32 v8, v8
	v_exp_f32_e32 v9, v9
	ds_read_b128 v[106:109], v89 offset:51200
	s_waitcnt lgkmcnt(2)
	v_mfma_f32_32x32x16_f16 v[18:33], v[122:125], v[76:79], v[18:33]
	v_exp_f32_e32 v13, v13
	v_exp_f32_e32 v11, v11
	ds_read_b128 v[122:125], v89 offset:54272
	s_waitcnt lgkmcnt(1)
	v_mfma_f32_32x32x16_f16 v[18:33], v[106:109], v[80:83], v[18:33]
	v_cvt_pk_bf16_f32 v107, v4, v5
	v_cvt_pk_bf16_f32 v106, v2, v3
	ds_read_b128 v[2:5], v89 offset:53248
	v_cvt_pk_bf16_f32 v109, v8, v9
	v_cvt_pk_bf16_f32 v108, v6, v7
	v_exp_f32_e32 v6, v10
	v_exp_f32_e32 v7, v12
	v_exp_f32_e32 v8, v14
	v_exp_f32_e32 v9, v16
	v_exp_f32_e32 v10, v17
	v_exp_f32_e32 v12, v15
	v_cvt_pk_bf16_f32 v115, v7, v13
	v_cvt_pk_bf16_f32 v114, v6, v11
	v_cvt_pk_bf16_f32 v117, v9, v10
	v_cvt_pk_bf16_f32 v116, v8, v12
	s_waitcnt lgkmcnt(0)
	v_mfma_f32_32x32x16_f16 v[2:17], v[2:5], v[72:75], 0
	v_permlane16_swap_b32_e32 v106, v114
	v_permlane16_swap_b32_e32 v107, v115
	v_permlane16_swap_b32_e32 v108, v116
	v_permlane16_swap_b32_e32 v109, v117
	v_mfma_f32_32x32x16_f16 v[2:17], v[122:125], v[76:79], v[2:17]
	v_exp_f32_e32 v18, v18
	v_exp_f32_e32 v20, v20
	v_exp_f32_e32 v21, v21
	v_exp_f32_e32 v19, v19
	v_exp_f32_e32 v22, v22
	v_exp_f32_e32 v24, v24
	v_exp_f32_e32 v25, v25
	v_mfma_f32_16x16x32_bf16 v[84:87], v[118:121], v[106:109], v[84:87]
	v_exp_f32_e32 v23, v23
	v_exp_f32_e32 v29, v29
	v_exp_f32_e32 v27, v27
	v_mfma_f32_16x16x32_bf16 v[34:37], v[118:121], v[114:117], v[34:37]
	ds_read_b128 v[106:109], v89 offset:55296
	ds_read_b128 v[114:117], v89 offset:56320
	ds_read_b128 v[122:125], v89 offset:58368
	s_waitcnt lgkmcnt(2)
	v_mfma_f32_32x32x16_f16 v[2:17], v[106:109], v[80:83], v[2:17]
	v_cvt_pk_bf16_f32 v107, v20, v21
	v_cvt_pk_bf16_f32 v106, v18, v19
	ds_read_b128 v[18:21], v89 offset:57344
	v_cvt_pk_bf16_f32 v109, v24, v25
	v_cvt_pk_bf16_f32 v108, v22, v23
	v_exp_f32_e32 v22, v26
	v_exp_f32_e32 v23, v28
	v_exp_f32_e32 v24, v30
	v_exp_f32_e32 v25, v32
	v_exp_f32_e32 v26, v33
	v_exp_f32_e32 v28, v31
	v_cvt_pk_bf16_f32 v119, v23, v29
	v_cvt_pk_bf16_f32 v118, v22, v27
	v_cvt_pk_bf16_f32 v121, v25, v26
	v_cvt_pk_bf16_f32 v120, v24, v28
	s_waitcnt lgkmcnt(0)
	v_mfma_f32_32x32x16_f16 v[18:33], v[18:21], v[72:75], 0
	v_permlane16_swap_b32_e32 v106, v118
	v_permlane16_swap_b32_e32 v107, v119
	v_permlane16_swap_b32_e32 v108, v120
	v_permlane16_swap_b32_e32 v109, v121
	v_mfma_f32_32x32x16_f16 v[18:33], v[122:125], v[76:79], v[18:33]
	v_exp_f32_e32 v2, v2
	v_exp_f32_e32 v4, v4
	v_exp_f32_e32 v5, v5
	v_exp_f32_e32 v3, v3
	v_exp_f32_e32 v6, v6
	v_exp_f32_e32 v8, v8
	v_exp_f32_e32 v9, v9
	v_mfma_f32_16x16x32_bf16 v[84:87], v[110:113], v[106:109], v[84:87]
	v_exp_f32_e32 v7, v7
	v_exp_f32_e32 v13, v13
	v_exp_f32_e32 v11, v11
	v_mfma_f32_16x16x32_bf16 v[34:37], v[110:113], v[118:121], v[34:37]
	ds_read_b128 v[106:109], v89 offset:59392
	ds_read_b128 v[110:113], v89 offset:60416
	ds_read_b128 v[122:125], v89 offset:62464
	s_waitcnt lgkmcnt(2)
	v_mfma_f32_32x32x16_f16 v[18:33], v[106:109], v[80:83], v[18:33]
	v_cvt_pk_bf16_f32 v107, v4, v5
	v_cvt_pk_bf16_f32 v106, v2, v3
	ds_read_b128 v[2:5], v89 offset:61440
	v_cvt_pk_bf16_f32 v109, v8, v9
	v_cvt_pk_bf16_f32 v108, v6, v7
	v_exp_f32_e32 v6, v10
	v_exp_f32_e32 v7, v12
	v_exp_f32_e32 v8, v14
	v_exp_f32_e32 v9, v16
	v_exp_f32_e32 v10, v17
	v_exp_f32_e32 v12, v15
	v_cvt_pk_bf16_f32 v119, v7, v13
	v_cvt_pk_bf16_f32 v118, v6, v11
	v_cvt_pk_bf16_f32 v121, v9, v10
	v_cvt_pk_bf16_f32 v120, v8, v12
	s_waitcnt lgkmcnt(0)
	v_mfma_f32_32x32x16_f16 v[40:55], v[2:5], v[72:75], 0
	v_permlane16_swap_b32_e32 v106, v118
	v_permlane16_swap_b32_e32 v107, v119
	v_permlane16_swap_b32_e32 v108, v120
	v_permlane16_swap_b32_e32 v109, v121
	v_mfma_f32_32x32x16_f16 v[40:55], v[122:125], v[76:79], v[40:55]
	v_exp_f32_e32 v38, v20
	v_exp_f32_e32 v20, v22
	v_exp_f32_e32 v22, v24
	v_exp_f32_e32 v24, v25
	v_exp_f32_e32 v25, v21
	v_exp_f32_e32 v23, v23
	v_exp_f32_e32 v39, v19
	v_mfma_f32_16x16x32_bf16 v[84:87], v[114:117], v[106:109], v[84:87]
	v_cvt_pk_bf16_f32 v21, v22, v24
	v_cvt_pk_bf16_f32 v19, v38, v25
	v_exp_f32_e32 v22, v26
	v_mfma_f32_16x16x32_bf16 v[34:37], v[114:117], v[118:121], v[34:37]
	ds_read_b128 v[106:109], v89 offset:63488
	ds_read_b128 v[56:59], v89 offset:64512
	v_exp_f32_e32 v25, v32
	v_exp_f32_e32 v26, v33
	s_waitcnt lgkmcnt(1)
	v_mfma_f32_32x32x16_f16 v[40:55], v[106:109], v[80:83], v[40:55]
	v_exp_f32_e32 v18, v18
	v_cvt_pk_bf16_f32 v20, v20, v23
	v_exp_f32_e32 v23, v28
	v_exp_f32_e32 v24, v30
	v_exp_f32_e32 v28, v31
	v_exp_f32_e32 v29, v29
	v_exp_f32_e32 v27, v27
	v_cvt_pk_bf16_f32 v25, v25, v26
	v_cvt_pk_bf16_f32 v18, v18, v39
	v_cvt_pk_bf16_f32 v24, v24, v28
	v_cvt_pk_bf16_f32 v23, v23, v29
	v_cvt_pk_bf16_f32 v22, v22, v27
	s_nop 1
	v_permlane16_swap_b32_e32 v18, v22
	v_permlane16_swap_b32_e32 v19, v23
	v_permlane16_swap_b32_e32 v20, v24
	v_permlane16_swap_b32_e32 v21, v25
	s_nop 1
	v_mfma_f32_16x16x32_bf16 v[18:21], v[110:113], v[18:21], v[84:87]
	v_mfma_f32_16x16x32_bf16 v[60:63], v[110:113], v[22:25], v[34:37]
	s_waitcnt lgkmcnt(0)
	s_waitcnt vmcnt(0)
	s_barrier
	s_cbranch_vccnz .LBB3_13

.LBB3_9:
	ds_read_b128 v[2:5], v89
	ds_read_b128 v[22:25], v89 offset:1024
	s_xor_b64 s[6:7], s[6:7], -1
	s_andn2_b64 vcc, exec, s[6:7]
	v_exp_f32_e32 v64, v42
	v_exp_f32_e32 v42, v44
	v_exp_f32_e32 v44, v46
	v_exp_f32_e32 v46, v47
	v_exp_f32_e32 v45, v45
	s_waitcnt lgkmcnt(1)
	v_mfma_f32_32x32x16_f16 v[2:17], v[2:5], v[72:75], 0
	v_exp_f32_e32 v47, v43
	v_exp_f32_e32 v40, v40
	v_exp_f32_e32 v65, v41
	v_cvt_pk_bf16_f32 v43, v44, v46
	v_cvt_pk_bf16_f32 v42, v42, v45
	s_waitcnt lgkmcnt(0)
	v_mfma_f32_32x32x16_f16 v[2:17], v[22:25], v[76:79], v[2:17]
	ds_read_b128 v[22:25], v89 offset:4096
	ds_read_b128 v[106:109], v89 offset:5120
	ds_read_b128 v[110:113], v89 offset:2048
	ds_read_b128 v[114:117], v89 offset:6144
	ds_read_b128 v[118:121], v89 offset:3072
	v_cvt_pk_bf16_f32 v41, v64, v47
	v_exp_f32_e32 v44, v48
	v_exp_f32_e32 v45, v50
	v_exp_f32_e32 v46, v52
	v_exp_f32_e32 v47, v54
	s_waitcnt lgkmcnt(4)
	v_mfma_f32_32x32x16_f16 v[24:39], v[22:25], v[72:75], 0
	v_exp_f32_e32 v48, v55
	v_exp_f32_e32 v50, v53
	v_exp_f32_e32 v51, v51
	v_exp_f32_e32 v49, v49
	v_cvt_pk_bf16_f32 v40, v40, v65
	s_waitcnt lgkmcnt(3)
	v_mfma_f32_32x32x16_f16 v[24:39], v[106:109], v[76:79], v[24:39]
	v_cvt_pk_bf16_f32 v47, v47, v48
	v_cvt_pk_bf16_f32 v46, v46, v50
	v_cvt_pk_bf16_f32 v45, v45, v51
	v_cvt_pk_bf16_f32 v44, v44, v49
	s_waitcnt lgkmcnt(2)
	v_mfma_f32_32x32x16_f16 v[2:17], v[110:113], v[80:83], v[2:17]
	v_permlane16_swap_b32_e32 v40, v44
	v_permlane16_swap_b32_e32 v41, v45
	v_permlane16_swap_b32_e32 v42, v46
	v_permlane16_swap_b32_e32 v43, v47
	s_waitcnt lgkmcnt(1)
	v_mfma_f32_32x32x16_f16 v[24:39], v[114:117], v[80:83], v[24:39]
	v_mfma_f32_16x16x32_bf16 v[84:87], v[56:59], v[40:43], v[18:21]
	v_mfma_f32_16x16x32_bf16 v[18:21], v[56:59], v[44:47], v[60:63]
	s_add_u32 m0, s48, 0x8000
	s_nop 0
	global_load_lds_dwordx4 v88, s[50:51]
	s_add_u32 s54, s50, 0x2000
	s_addc_u32 s55, s51, 0
	s_add_u32 m0, s48, 0xa000
	s_nop 0
	global_load_lds_dwordx4 v88, s[54:55]
	s_add_u32 s54, s50, 0x4000
	s_addc_u32 s55, s51, 0
	s_add_u32 m0, s48, 0xc000
	s_nop 0
	global_load_lds_dwordx4 v88, s[54:55]
	s_add_u32 s54, s50, 0x6000
	s_addc_u32 s55, s51, 0
	s_add_u32 m0, s48, 0xe000
	s_nop 0
	global_load_lds_dwordx4 v88, s[54:55]
	s_add_u32 s50, s50, 0x10000
	s_addc_u32 s51, s51, 0
	v_exp_f32_e32 v2, v2
	v_exp_f32_e32 v22, v3
	v_exp_f32_e32 v3, v4
	v_exp_f32_e32 v23, v5
	v_exp_f32_e32 v4, v6
	v_exp_f32_e32 v6, v7
	v_exp_f32_e32 v5, v8
	v_exp_f32_e32 v7, v9
	v_exp_f32_e32 v10, v10
	v_exp_f32_e32 v11, v11
	v_exp_f32_e32 v12, v12
	v_exp_f32_e32 v13, v13
	v_exp_f32_e32 v8, v14
	v_exp_f32_e32 v14, v15
	v_exp_f32_e32 v9, v16
	v_exp_f32_e32 v15, v17
	v_cvt_pk_bf16_f32 v5, v5, v7
	v_cvt_pk_bf16_f32 v4, v4, v6
	v_cvt_pk_bf16_f32 v3, v3, v23
	v_cvt_pk_bf16_f32 v2, v2, v22
	v_cvt_pk_bf16_f32 v9, v9, v15
	v_cvt_pk_bf16_f32 v8, v8, v14
	v_cvt_pk_bf16_f32 v7, v12, v13
	v_cvt_pk_bf16_f32 v6, v10, v11
	s_nop 1
	v_permlane16_swap_b32_e32 v2, v6
	v_permlane16_swap_b32_e32 v3, v7
	v_permlane16_swap_b32_e32 v4, v8
	v_permlane16_swap_b32_e32 v5, v9
	v_exp_f32_e32 v114, v24
	v_exp_f32_e32 v22, v26
	v_exp_f32_e32 v23, v28
	v_exp_f32_e32 v24, v30
	s_waitcnt lgkmcnt(0)
	v_mfma_f32_16x16x32_bf16 v[6:9], v[118:121], v[6:9], v[18:21]
	ds_read_b128 v[10:13], v89 offset:7168
	ds_read_b128 v[14:17], v89 offset:8192
	ds_read_b128 v[106:109], v89 offset:9216
	ds_read_b128 v[110:113], v89 offset:10240
	v_exp_f32_e32 v18, v31
	v_exp_f32_e32 v19, v29
	v_exp_f32_e32 v20, v27
	v_mfma_f32_16x16x32_bf16 v[2:5], v[118:121], v[2:5], v[84:87]
	s_nop 2
	v_exp_f32_e32 v84, v25
	v_cvt_pk_bf16_f32 v87, v24, v18
	v_cvt_pk_bf16_f32 v86, v23, v19
	v_cvt_pk_bf16_f32 v85, v22, v20
	s_waitcnt lgkmcnt(2)
	v_mfma_f32_32x32x16_f16 v[16:31], v[14:17], v[72:75], 0
	v_exp_f32_e32 v14, v32
	v_exp_f32_e32 v15, v34
	v_exp_f32_e32 v32, v36
	v_exp_f32_e32 v34, v37
	v_exp_f32_e32 v36, v38
	v_exp_f32_e32 v37, v39
	v_exp_f32_e32 v38, v35
	s_waitcnt lgkmcnt(1)
	v_mfma_f32_32x32x16_f16 v[16:31], v[106:109], v[76:79], v[16:31]
	v_exp_f32_e32 v39, v33
	v_cvt_pk_bf16_f32 v84, v114, v84
	v_cvt_pk_bf16_f32 v35, v36, v37
	v_cvt_pk_bf16_f32 v34, v32, v34
	v_cvt_pk_bf16_f32 v33, v15, v38
	v_cvt_pk_bf16_f32 v32, v14, v39
	s_nop 1
	v_permlane16_swap_b32_e32 v84, v32
	v_permlane16_swap_b32_e32 v85, v33
	v_permlane16_swap_b32_e32 v86, v34
	v_permlane16_swap_b32_e32 v87, v35
	ds_read_b128 v[36:39], v89 offset:11264
	s_nop 0
	v_mfma_f32_16x16x32_bf16 v[84:87], v[10:13], v[84:87], v[2:5]
	s_nop 2
	ds_read_b128 v[2:5], v89 offset:12288
	s_waitcnt lgkmcnt(2)
	v_mfma_f32_32x32x16_f16 v[16:31], v[110:113], v[80:83], v[16:31]
	v_mfma_f32_16x16x32_bf16 v[106:109], v[10:13], v[32:35], v[6:9]
	s_nop 10
	v_exp_f32_e32 v114, v16
	v_exp_f32_e32 v118, v17
	v_exp_f32_e32 v18, v18
	s_waitcnt lgkmcnt(0)
	v_mfma_f32_32x32x16_f16 v[2:17], v[2:5], v[72:75], 0
	v_exp_f32_e32 v20, v20
	v_exp_f32_e32 v21, v21
	v_exp_f32_e32 v19, v19
	ds_read_b128 v[32:35], v89 offset:13312
	ds_read_b128 v[110:113], v89 offset:14336
	v_cvt_pk_bf16_f32 v114, v114, v118
	v_cvt_pk_bf16_f32 v116, v20, v21
	v_cvt_pk_bf16_f32 v115, v18, v19
	ds_read_b128 v[118:121], v89 offset:15360
	ds_read_b128 v[18:21], v89 offset:16384
	v_exp_f32_e32 v22, v22
	v_exp_f32_e32 v23, v23
	s_waitcnt lgkmcnt(3)
	v_mfma_f32_32x32x16_f16 v[2:17], v[32:35], v[76:79], v[2:17]
	v_exp_f32_e32 v29, v29
	v_exp_f32_e32 v27, v27
	v_cvt_pk_bf16_f32 v117, v22, v23
	v_exp_f32_e32 v22, v24
	v_exp_f32_e32 v23, v26
	v_exp_f32_e32 v24, v28
	v_exp_f32_e32 v26, v30
	v_exp_f32_e32 v28, v31
	v_exp_f32_e32 v25, v25
	ds_read_b128 v[122:125], v89 offset:17408
	s_waitcnt lgkmcnt(3)
	v_mfma_f32_32x32x16_f16 v[2:17], v[110:113], v[80:83], v[2:17]
	v_cvt_pk_bf16_f32 v113, v26, v28
	v_cvt_pk_bf16_f32 v112, v24, v29
	v_cvt_pk_bf16_f32 v111, v23, v27
	v_cvt_pk_bf16_f32 v110, v22, v25
	s_nop 1
	v_permlane16_swap_b32_e32 v114, v110
	v_permlane16_swap_b32_e32 v115, v111
	s_waitcnt lgkmcnt(1)
	v_mfma_f32_32x32x16_f16 v[18:33], v[18:21], v[72:75], 0
	v_permlane16_swap_b32_e32 v116, v112
	v_permlane16_swap_b32_e32 v117, v113
	v_exp_f32_e32 v2, v2
	v_exp_f32_e32 v4, v4
	v_exp_f32_e32 v5, v5
	v_mfma_f32_16x16x32_bf16 v[84:87], v[36:39], v[114:117], v[84:87]
	v_exp_f32_e32 v3, v3
	v_exp_f32_e32 v6, v6
	v_exp_f32_e32 v7, v7
	v_mfma_f32_16x16x32_bf16 v[34:37], v[36:39], v[110:113], v[106:109]
	ds_read_b128 v[110:113], v89 offset:19456
	v_exp_f32_e32 v8, v8
	v_exp_f32_e32 v9, v9
	ds_read_b128 v[106:109], v89 offset:18432
	s_waitcnt lgkmcnt(2)
	v_mfma_f32_32x32x16_f16 v[18:33], v[122:125], v[76:79], v[18:33]
	v_exp_f32_e32 v13, v13
	v_exp_f32_e32 v11, v11
	ds_read_b128 v[122:125], v89 offset:21504
	s_waitcnt lgkmcnt(1)
	v_mfma_f32_32x32x16_f16 v[18:33], v[106:109], v[80:83], v[18:33]
	v_cvt_pk_bf16_f32 v107, v4, v5
	v_cvt_pk_bf16_f32 v106, v2, v3
	ds_read_b128 v[2:5], v89 offset:20480
	v_cvt_pk_bf16_f32 v109, v8, v9
	v_cvt_pk_bf16_f32 v108, v6, v7
	v_exp_f32_e32 v6, v10
	v_exp_f32_e32 v7, v12
	v_exp_f32_e32 v8, v14
	v_exp_f32_e32 v9, v16
	v_exp_f32_e32 v10, v17
	v_exp_f32_e32 v12, v15
	v_cvt_pk_bf16_f32 v115, v7, v13
	v_cvt_pk_bf16_f32 v114, v6, v11
	v_cvt_pk_bf16_f32 v117, v9, v10
	v_cvt_pk_bf16_f32 v116, v8, v12
	s_waitcnt lgkmcnt(0)
	v_mfma_f32_32x32x16_f16 v[2:17], v[2:5], v[72:75], 0
	v_permlane16_swap_b32_e32 v106, v114
	v_permlane16_swap_b32_e32 v107, v115
	v_permlane16_swap_b32_e32 v108, v116
	v_permlane16_swap_b32_e32 v109, v117
	v_mfma_f32_32x32x16_f16 v[2:17], v[122:125], v[76:79], v[2:17]
	v_exp_f32_e32 v18, v18
	v_exp_f32_e32 v20, v20
	v_exp_f32_e32 v21, v21
	v_exp_f32_e32 v19, v19
	v_exp_f32_e32 v22, v22
	v_exp_f32_e32 v24, v24
	v_exp_f32_e32 v25, v25
	v_mfma_f32_16x16x32_bf16 v[84:87], v[118:121], v[106:109], v[84:87]
	v_exp_f32_e32 v23, v23
	v_exp_f32_e32 v29, v29
	v_exp_f32_e32 v27, v27
	v_mfma_f32_16x16x32_bf16 v[34:37], v[118:121], v[114:117], v[34:37]
	ds_read_b128 v[106:109], v89 offset:22528
	ds_read_b128 v[114:117], v89 offset:23552
	ds_read_b128 v[122:125], v89 offset:25600
	s_waitcnt lgkmcnt(2)
	v_mfma_f32_32x32x16_f16 v[2:17], v[106:109], v[80:83], v[2:17]
	v_cvt_pk_bf16_f32 v107, v20, v21
	v_cvt_pk_bf16_f32 v106, v18, v19
	ds_read_b128 v[18:21], v89 offset:24576
	v_cvt_pk_bf16_f32 v109, v24, v25
	v_cvt_pk_bf16_f32 v108, v22, v23
	v_exp_f32_e32 v22, v26
	v_exp_f32_e32 v23, v28
	v_exp_f32_e32 v24, v30
	v_exp_f32_e32 v25, v32
	v_exp_f32_e32 v26, v33
	v_exp_f32_e32 v28, v31
	v_cvt_pk_bf16_f32 v119, v23, v29
	v_cvt_pk_bf16_f32 v118, v22, v27
	v_cvt_pk_bf16_f32 v121, v25, v26
	v_cvt_pk_bf16_f32 v120, v24, v28
	s_waitcnt lgkmcnt(0)
	v_mfma_f32_32x32x16_f16 v[18:33], v[18:21], v[72:75], 0
	v_permlane16_swap_b32_e32 v106, v118
	v_permlane16_swap_b32_e32 v107, v119
	v_permlane16_swap_b32_e32 v108, v120
	v_permlane16_swap_b32_e32 v109, v121
	v_mfma_f32_32x32x16_f16 v[18:33], v[122:125], v[76:79], v[18:33]
	v_exp_f32_e32 v2, v2
	v_exp_f32_e32 v4, v4
	v_exp_f32_e32 v5, v5
	v_exp_f32_e32 v3, v3
	v_exp_f32_e32 v6, v6
	v_exp_f32_e32 v8, v8
	v_exp_f32_e32 v9, v9
	v_mfma_f32_16x16x32_bf16 v[84:87], v[110:113], v[106:109], v[84:87]
	v_exp_f32_e32 v7, v7
	v_exp_f32_e32 v13, v13
	v_exp_f32_e32 v11, v11
	v_mfma_f32_16x16x32_bf16 v[34:37], v[110:113], v[118:121], v[34:37]
	ds_read_b128 v[106:109], v89 offset:26624
	ds_read_b128 v[110:113], v89 offset:27648
	ds_read_b128 v[122:125], v89 offset:29696
	s_waitcnt lgkmcnt(2)
	v_mfma_f32_32x32x16_f16 v[18:33], v[106:109], v[80:83], v[18:33]
	v_cvt_pk_bf16_f32 v107, v4, v5
	v_cvt_pk_bf16_f32 v106, v2, v3
	ds_read_b128 v[2:5], v89 offset:28672
	v_cvt_pk_bf16_f32 v109, v8, v9
	v_cvt_pk_bf16_f32 v108, v6, v7
	v_exp_f32_e32 v6, v10
	v_exp_f32_e32 v7, v12
	v_exp_f32_e32 v8, v14
	v_exp_f32_e32 v9, v16
	v_exp_f32_e32 v10, v17
	v_exp_f32_e32 v12, v15
	v_cvt_pk_bf16_f32 v119, v7, v13
	v_cvt_pk_bf16_f32 v118, v6, v11
	v_cvt_pk_bf16_f32 v121, v9, v10
	v_cvt_pk_bf16_f32 v120, v8, v12
	s_waitcnt lgkmcnt(0)
	v_mfma_f32_32x32x16_f16 v[40:55], v[2:5], v[72:75], 0
	v_permlane16_swap_b32_e32 v106, v118
	v_permlane16_swap_b32_e32 v107, v119
	v_permlane16_swap_b32_e32 v108, v120
	v_permlane16_swap_b32_e32 v109, v121
	v_mfma_f32_32x32x16_f16 v[40:55], v[122:125], v[76:79], v[40:55]
	v_exp_f32_e32 v38, v20
	v_exp_f32_e32 v20, v22
	v_exp_f32_e32 v22, v24
	v_exp_f32_e32 v24, v25
	v_exp_f32_e32 v25, v21
	v_exp_f32_e32 v23, v23
	v_exp_f32_e32 v39, v19
	v_mfma_f32_16x16x32_bf16 v[84:87], v[114:117], v[106:109], v[84:87]
	v_cvt_pk_bf16_f32 v21, v22, v24
	v_cvt_pk_bf16_f32 v19, v38, v25
	v_exp_f32_e32 v22, v26
	v_mfma_f32_16x16x32_bf16 v[34:37], v[114:117], v[118:121], v[34:37]
	ds_read_b128 v[106:109], v89 offset:30720
	ds_read_b128 v[56:59], v89 offset:31744
	v_exp_f32_e32 v25, v32
	v_exp_f32_e32 v26, v33
	s_waitcnt lgkmcnt(1)
	v_mfma_f32_32x32x16_f16 v[40:55], v[106:109], v[80:83], v[40:55]
	v_exp_f32_e32 v18, v18
	v_cvt_pk_bf16_f32 v20, v20, v23
	v_exp_f32_e32 v23, v28
	v_exp_f32_e32 v24, v30
	v_exp_f32_e32 v28, v31
	v_exp_f32_e32 v29, v29
	v_exp_f32_e32 v27, v27
	v_cvt_pk_bf16_f32 v25, v25, v26
	v_cvt_pk_bf16_f32 v18, v18, v39
	v_cvt_pk_bf16_f32 v24, v24, v28
	v_cvt_pk_bf16_f32 v23, v23, v29
	v_cvt_pk_bf16_f32 v22, v22, v27
	s_nop 1
	v_permlane16_swap_b32_e32 v18, v22
	v_permlane16_swap_b32_e32 v19, v23
	v_permlane16_swap_b32_e32 v20, v24
	v_permlane16_swap_b32_e32 v21, v25
	s_nop 1
	v_mfma_f32_16x16x32_bf16 v[18:21], v[110:113], v[18:21], v[84:87]
	v_mfma_f32_16x16x32_bf16 v[60:63], v[110:113], v[22:25], v[34:37]
	s_waitcnt lgkmcnt(0)
	s_waitcnt vmcnt(0)
	s_barrier
	s_branch .LBB3_6
.LBB3_13:
	v_exp_f32_e32 v64, v42
	v_exp_f32_e32 v42, v44
	v_exp_f32_e32 v44, v46
	v_exp_f32_e32 v46, v47
	v_exp_f32_e32 v45, v45
	v_exp_f32_e32 v47, v43
	v_exp_f32_e32 v40, v40
	v_exp_f32_e32 v65, v41
	v_cvt_pk_bf16_f32 v43, v44, v46
	v_cvt_pk_bf16_f32 v42, v42, v45
	v_cvt_pk_bf16_f32 v41, v64, v47
	v_exp_f32_e32 v44, v48
	v_exp_f32_e32 v45, v50
	v_exp_f32_e32 v46, v52
	v_exp_f32_e32 v47, v54
	v_exp_f32_e32 v48, v55
	v_exp_f32_e32 v50, v53
	v_exp_f32_e32 v51, v51
	v_exp_f32_e32 v49, v49
	v_cvt_pk_bf16_f32 v40, v40, v65
	v_cvt_pk_bf16_f32 v47, v47, v48
	v_cvt_pk_bf16_f32 v46, v46, v50
	v_cvt_pk_bf16_f32 v45, v45, v51
	v_cvt_pk_bf16_f32 v44, v44, v49
	s_nop 1
	v_permlane16_swap_b32_e32 v40, v44
	v_permlane16_swap_b32_e32 v41, v45
	v_permlane16_swap_b32_e32 v42, v46
	v_permlane16_swap_b32_e32 v43, v47
	s_nop 1
	v_mfma_f32_16x16x32_bf16 v[84:87], v[56:59], v[40:43], v[18:21]
	v_mfma_f32_16x16x32_bf16 v[18:21], v[56:59], v[44:47], v[60:63]
	s_lshl_b32 s3, s3, 14
	s_add_i32 s24, s24, s3
	v_and_or_b32 v2, v0, 15, s24
	v_mad_u64_u32 v[2:3], s[4:5], v2, 48, s[20:21]
	v_lshrrev_b32_e32 v4, 4, v1
	v_cmp_lt_u32_e32 vcc, 31, v1
	s_and_saveexec_b64 s[4:5], vcc
	s_xor_b64 s[4:5], exec, s[4:5]
	s_cbranch_execz .LBB3_17
	v_cmp_eq_u32_e32 vcc, 2, v4
	s_and_saveexec_b64 s[6:7], vcc
	s_cbranch_execz .LBB3_16
	global_store_dword v[2:3], v84, off offset:32
	global_store_dword v[2:3], v18, off offset:800
